# GEMM phase prologue: K-tile 1's three half-tile LDS-DMA requests issued ahead of K-tile 0's first wait (vmcnt(2) -> vmcnt(8)) instead of after its barrier
# speedup vs baseline: 1.0196x; 1.0196x over previous
.LBB0_172:
	s_add_u32 s8, s46, 0x8e00000
	s_addc_u32 s9, s47, 0
	s_lshl_b32 s10, s10, 5
	s_and_b32 s16, s10, 0x60
	s_mov_b64 s[10:11], 0x80
	s_add_i32 m0, s23, 0x18000
	v_lshl_add_u64 v[8:9], v[8:9], 0, s[10:11]
	s_lshl_b32 s13, s12, 13
	s_lshl_b32 s17, s16, 7
	global_load_lds_dwordx4 v[8:9], off
	v_lshl_add_u64 v[6:7], v[6:7], 0, s[10:11]
	s_add_i32 m0, s23, 0x1a000
	s_add_i32 s39, s23, 0x8000
	s_add_i32 s40, s23, 0xa000
	global_load_lds_dwordx4 v[6:7], off
	v_lshl_add_u64 v[2:3], v[2:3], 0, s[10:11]
	s_mov_b32 m0, s39
	s_add_u32 s14, s26, 0x80080
	global_load_lds_dwordx4 v[2:3], off
	v_lshl_add_u64 v[2:3], v[4:5], 0, s[10:11]
	s_mov_b32 m0, s40
	s_addc_u32 s15, s27, 0
	global_load_lds_dwordx4 v[2:3], off
	s_add_i32 m0, s23, 0x1c000
	v_lshl_add_u64 v[2:3], s[14:15], 0, v[134:135]
	global_load_lds_dwordx4 v[2:3], off
	v_lshl_add_u64 v[2:3], s[14:15], 0, v[130:131]
	s_add_i32 m0, s23, 0x1e000
	s_sext_i32_i16 s45, s4
	global_load_lds_dwordx4 v[2:3], off
	s_waitcnt vmcnt(8)
	s_barrier
	v_and_b32_e32 v2, 15, v0
	v_lshlrev_b32_e32 v3, 1, v13
	v_lshlrev_b32_e32 v4, 2, v0
	v_lshlrev_b32_e32 v5, 6, v0
	s_movk_i32 s4, 0x3c0
	v_lshl_or_b32 v152, s12, 6, v2
	v_lshl_or_b32 v2, v2, 6, v3
	v_and_b32_e32 v4, 32, v4
	v_and_or_b32 v3, v5, s4, v3
	v_bitop3_b32 v153, s17, v3, v4 bitop3:0xf6
	v_lshlrev_b32_e32 v3, 9, v0
	v_bitop3_b32 v2, v2, s13, v4 bitop3:0xde
	v_and_b32_e32 v3, 0x30000, v3
	v_lshlrev_b32_e32 v4, 12, v14
	v_or3_b32 v3, v11, v3, v4
	v_add_u32_e32 v138, v3, v12
	v_lshlrev_b32_e32 v3, 5, v10
	s_waitcnt vmcnt(6)
	s_cmpk_lt_u32 s5, 0x100
	v_and_b32_e32 v3, 0x70000, v3
	s_cselect_b64 s[12:13], -1, 0
	v_or3_b32 v3, v11, v3, v4
	s_add_i32 s42, 0, 0x10000
	s_add_i32 s43, 0, 0x14000
	s_ashr_i32 s41, s88, 31
	v_or_b32_e32 v154, s16, v13
	v_mov_b32_e32 v139, v135
	v_add_u32_e32 v140, v3, v12
	v_mov_b32_e32 v141, v135
	v_mov_b64_e32 v[142:143], 0x500
	v_mov_b64_e32 v[144:145], 0x4ff
	v_add_u32_e32 v155, s42, v153
	v_add_u32_e32 v156, s43, v153
	v_add_u32_e32 v157, 0, v2
	s_movk_i32 s44, 0x2800
	s_barrier
	s_waitcnt vmcnt(0)
	s_branch .LBB0_175

.LBB0_374:
	s_add_u32 s10, s46, 0x500000
	s_addc_u32 s11, s47, 0
	s_lshl_b32 s5, s5, 5
	s_mov_b64 s[12:13], 0x80
	s_and_b32 s16, s5, 0x60
	s_add_i32 m0, s27, 0x18000
	v_lshl_add_u64 v[8:9], v[8:9], 0, s[12:13]
	s_lshl_b32 s15, s4, 13
	s_lshl_b32 s5, s16, 7
	global_load_lds_dwordx4 v[8:9], off
	v_lshl_add_u64 v[6:7], v[6:7], 0, s[12:13]
	s_add_i32 m0, s27, 0x1a000
	s_add_i32 s41, s27, 0x8000
	s_add_i32 s42, s27, 0xa000
	global_load_lds_dwordx4 v[6:7], off
	v_lshl_add_u64 v[2:3], v[2:3], 0, s[12:13]
	s_mov_b32 m0, s41
	s_add_u32 s6, s30, 0x80080
	global_load_lds_dwordx4 v[2:3], off
	v_lshl_add_u64 v[2:3], v[4:5], 0, s[12:13]
	s_mov_b32 m0, s42
	s_addc_u32 s7, s31, 0
	global_load_lds_dwordx4 v[2:3], off
	s_add_i32 m0, s27, 0x1c000
	v_lshl_add_u64 v[2:3], s[6:7], 0, v[132:133]
	global_load_lds_dwordx4 v[2:3], off
	v_lshl_add_u64 v[2:3], s[6:7], 0, v[136:137]
	s_add_i32 m0, s27, 0x1e000
	v_lshlrev_b32_e32 v5, 2, v0
	global_load_lds_dwordx4 v[2:3], off
	s_waitcnt vmcnt(8)
	s_barrier
	v_and_b32_e32 v2, 15, v0
	v_bfe_u32 v3, v0, 4, 2
	v_lshl_or_b32 v152, s4, 6, v2
	v_lshlrev_b32_e32 v4, 4, v3
	v_lshlrev_b32_e32 v6, 6, v0
	s_movk_i32 s4, 0x3c0
	v_lshl_or_b32 v2, v2, 6, v4
	v_and_b32_e32 v5, 32, v5
	v_and_or_b32 v4, v6, s4, v4
	v_bitop3_b32 v153, s5, v4, v5 bitop3:0xf6
	v_cmp_eq_u32_e64 s[4:5], 0, v3
	v_lshl_or_b32 v154, v3, 3, s16
	v_lshlrev_b32_e32 v3, 9, v0
	v_and_b32_e32 v3, 0x30000, v3
	v_lshlrev_b32_e32 v4, 12, v12
	v_or3_b32 v3, v10, v3, v4
	v_add_u32_e32 v138, v3, v11
	v_lshlrev_b32_e32 v3, 5, v13
	v_bitop3_b32 v2, v2, s15, v5 bitop3:0xde
	s_waitcnt vmcnt(6)
	s_cmpk_lt_u32 s14, 0x100
	v_and_b32_e32 v3, 0x70000, v3
	s_cselect_b64 s[14:15], -1, 0
	v_or3_b32 v3, v10, v3, v4
	s_add_i32 s45, 0, 0x10000
	s_add_i32 s54, 0, 0x14000
	v_add_u32_e32 v157, 0, v2
	v_mbcnt_lo_u32_b32 v2, -1, 0
	s_ashr_i32 s43, s88, 31
	s_ashr_i32 s44, s97, 31
	v_mov_b32_e32 v139, v133
	v_add_u32_e32 v140, v3, v11
	v_mov_b32_e32 v141, v133
	v_mov_b64_e32 v[142:143], 0x200
	v_mov_b64_e32 v[144:145], 0x1ff
	v_add_u32_e32 v155, s45, v153
	v_add_u32_e32 v156, s54, v153
	v_mbcnt_hi_u32_b32 v159, -1, v2
	s_mov_b32 s55, 0x49800000
	s_barrier
	s_branch .LBB0_377

.LBB0_465:
	s_add_u32 s8, s46, 0x8e00000
	s_addc_u32 s9, s47, 0
	s_add_u32 s10, s46, 0x500000
	s_addc_u32 s11, s47, 0
	s_lshl_b32 s12, s12, 5
	s_and_b32 s18, s12, 0x60
	s_mov_b64 s[12:13], 0x80
	s_add_i32 m0, s25, 0x18000
	v_lshl_add_u64 v[8:9], v[8:9], 0, s[12:13]
	s_lshl_b32 s15, s14, 13
	s_lshl_b32 s19, s18, 7
	global_load_lds_dwordx4 v[8:9], off
	v_lshl_add_u64 v[6:7], v[6:7], 0, s[12:13]
	s_add_i32 m0, s25, 0x1a000
	s_add_i32 s41, s25, 0x8000
	s_add_i32 s42, s25, 0xa000
	global_load_lds_dwordx4 v[6:7], off
	v_lshl_add_u64 v[2:3], v[2:3], 0, s[12:13]
	s_mov_b32 m0, s41
	s_add_u32 s16, s28, 0x80080
	global_load_lds_dwordx4 v[2:3], off
	v_lshl_add_u64 v[2:3], v[4:5], 0, s[12:13]
	s_mov_b32 m0, s42
	s_addc_u32 s17, s29, 0
	global_load_lds_dwordx4 v[2:3], off
	s_add_i32 m0, s25, 0x1c000
	v_lshl_add_u64 v[2:3], s[16:17], 0, v[134:135]
	global_load_lds_dwordx4 v[2:3], off
	v_lshl_add_u64 v[2:3], s[16:17], 0, v[130:131]
	s_add_i32 m0, s25, 0x1e000
	s_sext_i32_i16 s54, s4
	global_load_lds_dwordx4 v[2:3], off
	s_waitcnt vmcnt(8)
	s_barrier
	v_and_b32_e32 v2, 15, v0
	v_lshlrev_b32_e32 v3, 1, v13
	v_lshlrev_b32_e32 v4, 2, v0
	v_lshlrev_b32_e32 v5, 6, v0
	s_movk_i32 s4, 0x3c0
	v_lshl_or_b32 v156, s14, 6, v2
	v_lshl_or_b32 v2, v2, 6, v3
	v_and_b32_e32 v4, 32, v4
	v_and_or_b32 v3, v5, s4, v3
	v_bitop3_b32 v157, s19, v3, v4 bitop3:0xf6
	v_lshlrev_b32_e32 v3, 9, v0
	v_bitop3_b32 v2, v2, s15, v4 bitop3:0xde
	v_and_b32_e32 v3, 0x30000, v3
	v_lshlrev_b32_e32 v4, 12, v14
	v_or3_b32 v3, v11, v3, v4
	v_add_u32_e32 v138, v3, v12
	v_lshlrev_b32_e32 v3, 5, v10
	s_waitcnt vmcnt(6)
	s_cmpk_lt_u32 s5, 0x100
	v_and_b32_e32 v3, 0x70000, v3
	s_cselect_b64 s[14:15], -1, 0
	v_or3_b32 v3, v11, v3, v4
	s_add_i32 s44, 0, 0x10000
	s_add_i32 s45, 0, 0x14000
	s_ashr_i32 s43, s88, 31
	v_or_b32_e32 v159, s18, v13
	v_mov_b32_e32 v139, v135
	v_add_u32_e32 v140, v3, v12
	v_mov_b32_e32 v141, v135
	v_mov_b64_e32 v[142:143], 0xb00
	v_mov_b64_e32 v[144:145], 0xaff
	v_add_u32_e32 v160, s44, v157
	v_add_u32_e32 v161, s45, v157
	v_add_u32_e32 v162, 0, v2
	s_movk_i32 s48, 0x1600
	v_mov_b32_e32 v163, 0x358637bd
	s_mov_b32 s49, 0xc3e00000
	v_mov_b32_e32 v164, 0x43e00000
	s_barrier
	s_branch .LBB0_468

.LBB0_542:
	s_add_u32 s12, s46, 0x520000
	s_addc_u32 s13, s47, 0
	s_lshl_b32 s1, s1, 5
	s_mov_b64 s[14:15], 0x80
	s_and_b32 s1, s1, 0x60
	s_add_i32 m0, s30, 0x18000
	v_lshl_add_u64 v[8:9], v[8:9], 0, s[14:15]
	s_lshl_b32 s7, s0, 13
	s_lshl_b32 s16, s1, 7
	global_load_lds_dwordx4 v[8:9], off
	v_lshl_add_u64 v[6:7], v[6:7], 0, s[14:15]
	s_add_i32 m0, s30, 0x1a000
	s_add_i32 s36, s30, 0x8000
	s_add_i32 s37, s30, 0xa000
	global_load_lds_dwordx4 v[6:7], off
	v_lshl_add_u64 v[2:3], v[2:3], 0, s[14:15]
	s_mov_b32 m0, s36
	s_add_u32 s4, s22, 0xb0080
	global_load_lds_dwordx4 v[2:3], off
	v_lshl_add_u64 v[2:3], v[4:5], 0, s[14:15]
	s_mov_b32 m0, s37
	s_addc_u32 s5, s23, 0
	global_load_lds_dwordx4 v[2:3], off
	s_add_i32 m0, s30, 0x1c000
	v_lshl_add_u64 v[2:3], s[4:5], 0, v[132:133]
	global_load_lds_dwordx4 v[2:3], off
	v_lshl_add_u64 v[2:3], s[4:5], 0, v[136:137]
	s_add_i32 m0, s30, 0x1e000
	v_lshlrev_b32_e32 v5, 2, v0
	global_load_lds_dwordx4 v[2:3], off
	s_waitcnt vmcnt(8)
	s_barrier
	v_bfe_u32 v3, v0, 4, 2
	v_and_b32_e32 v2, 15, v0
	v_lshlrev_b32_e32 v4, 4, v3
	v_lshl_or_b32 v152, s0, 6, v2
	v_lshl_or_b32 v2, v2, 6, v4
	v_and_b32_e32 v5, 32, v5
	v_lshlrev_b32_e32 v6, 6, v0
	s_movk_i32 s0, 0x3c0
	v_bitop3_b32 v2, v2, s7, v5 bitop3:0xde
	v_and_or_b32 v4, v6, s0, v4
	s_waitcnt vmcnt(6)
	s_cmpk_lt_u32 s6, 0x100
	v_cmp_eq_u32_e64 s[4:5], 0, v3
	v_lshl_or_b32 v154, v3, 3, s1
	v_add_u16_e32 v3, v10, v11
	v_bitop3_b32 v153, s16, v4, v5 bitop3:0xf6
	s_cselect_b64 s[16:17], -1, 0
	v_lshrrev_b16_e32 v3, 1, v3
	s_add_i32 s40, 0, 0x10000
	s_add_i32 s41, 0, 0x14000
	v_add_u32_e32 v157, 0, v2
	v_mbcnt_lo_u32_b32 v2, -1, 0
	s_ashr_i32 s38, s88, 31
	s_ashr_i32 s39, s97, 31
	v_add_lshl_u32 v138, v12, v3, 1
	v_mov_b32_e32 v139, v133
	v_add_lshl_u32 v140, v13, v3, 1
	v_mov_b32_e32 v141, v133
	v_mov_b64_e32 v[142:143], 0x200
	v_mov_b64_e32 v[144:145], 0x1ff
	v_add_u32_e32 v155, s40, v153
	v_add_u32_e32 v156, s41, v153
	v_mov_b32_e32 v159, 0x7c7c7c7c
	v_mov_b32_e32 v160, 0x78787878
	v_mbcnt_hi_u32_b32 v161, -1, v2
	s_mov_b32 s42, 0x49800000
	s_barrier
	s_branch .LBB0_545

.LBB0_641:
	s_add_u32 s10, s46, 0x8e00000
	s_addc_u32 s11, s47, 0
	s_add_u32 s12, s46, 0x520000
	s_addc_u32 s13, s47, 0
	s_lshl_b32 s1, s14, 5
	s_mov_b64 s[14:15], 0x80
	s_and_b32 s20, s1, 0x60
	s_add_i32 m0, s42, 0x18000
	v_lshl_add_u64 v[8:9], v[8:9], 0, s[14:15]
	s_lshl_b32 s17, s16, 13
	s_lshl_b32 s21, s20, 7
	global_load_lds_dwordx4 v[8:9], off
	v_lshl_add_u64 v[6:7], v[6:7], 0, s[14:15]
	s_add_i32 m0, s42, 0x1a000
	s_add_i32 s49, s42, 0x8000
	s_add_i32 s54, s42, 0xa000
	global_load_lds_dwordx4 v[6:7], off
	v_lshl_add_u64 v[2:3], v[2:3], 0, s[14:15]
	s_mov_b32 m0, s49
	s_add_u32 s18, s36, 0x80080
	global_load_lds_dwordx4 v[2:3], off
	v_lshl_add_u64 v[2:3], v[4:5], 0, s[14:15]
	s_mov_b32 m0, s54
	s_addc_u32 s19, s37, 0
	global_load_lds_dwordx4 v[2:3], off
	s_add_i32 m0, s42, 0x1c000
	v_lshl_add_u64 v[2:3], s[18:19], 0, v[132:133]
	global_load_lds_dwordx4 v[2:3], off
	v_lshl_add_u64 v[2:3], s[18:19], 0, v[136:137]
	s_add_i32 m0, s42, 0x1e000
	s_sext_i32_i16 s1, s4
	global_load_lds_dwordx4 v[2:3], off
	s_waitcnt vmcnt(8)
	s_barrier
	v_and_b32_e32 v2, 15, v0
	v_lshlrev_b32_e32 v3, 1, v13
	v_lshlrev_b32_e32 v4, 2, v0
	v_lshlrev_b32_e32 v5, 6, v0
	s_movk_i32 s4, 0x3c0
	v_lshl_or_b32 v154, s16, 6, v2
	v_lshl_or_b32 v2, v2, 6, v3
	v_and_b32_e32 v4, 32, v4
	v_and_or_b32 v3, v5, s4, v3
	v_bitop3_b32 v155, s21, v3, v4 bitop3:0xf6
	v_lshlrev_b32_e32 v3, 9, v0
	v_bitop3_b32 v2, v2, s17, v4 bitop3:0xde
	v_and_b32_e32 v3, 0x30000, v3
	v_lshlrev_b32_e32 v4, 12, v12
	v_or3_b32 v3, v10, v3, v4
	v_add_u32_e32 v138, v3, v11
	v_lshlrev_b32_e32 v3, 5, v14
	s_waitcnt vmcnt(6)
	s_cmpk_lt_u32 s5, 0x100
	v_and_b32_e32 v3, 0x70000, v3
	s_cselect_b64 s[16:17], -1, 0
	v_or3_b32 v3, v10, v3, v4
	s_add_i32 s56, 0, 0x10000
	s_add_i32 s57, 0, 0x14000
	s_ashr_i32 s55, s88, 31
	v_or_b32_e32 v156, s20, v13
	v_mov_b32_e32 v139, v133
	v_add_u32_e32 v140, v3, v11
	v_mov_b32_e32 v141, v133
	v_mov_b64_e32 v[142:143], 0x800
	v_mov_b64_e32 v[144:145], 0x7ff
	v_add_u32_e32 v157, s56, v155
	v_add_u32_e32 v159, s57, v155
	v_add_u32_e32 v160, 0, v2
	v_mov_b32_e32 v161, 0x358637bd
	s_mov_b32 s58, 0x200000
	s_mov_b64 s[18:19], 0x240000
	s_mov_b32 s59, 0x240000
	s_mov_b64 s[20:21], 0x280000
	s_mov_b32 s60, 0x280000
	s_mov_b64 s[22:23], 0x2c0000
	s_mov_b32 s61, 0x2c0000
	s_barrier
	s_branch .LBB0_644

.LBB0_838:
	s_lshl_b32 s8, s8, 5
	s_and_b32 s14, s8, 0x60
	s_mov_b64 s[8:9], 0x80
	s_add_i32 m0, s31, 0x18000
	v_lshl_add_u64 v[8:9], v[8:9], 0, s[8:9]
	s_lshl_b32 s11, s5, 13
	s_lshl_b32 s15, s14, 7
	global_load_lds_dwordx4 v[8:9], off
	v_lshl_add_u64 v[6:7], v[6:7], 0, s[8:9]
	s_add_i32 m0, s31, 0x1a000
	s_add_i32 s48, s31, 0x8000
	s_add_i32 s49, s31, 0xa000
	global_load_lds_dwordx4 v[6:7], off
	v_lshl_add_u64 v[2:3], v[2:3], 0, s[8:9]
	s_mov_b32 m0, s48
	s_add_u32 s12, s36, 0x80080
	global_load_lds_dwordx4 v[2:3], off
	v_lshl_add_u64 v[2:3], v[4:5], 0, s[8:9]
	s_mov_b32 m0, s49
	s_addc_u32 s13, s37, 0
	global_load_lds_dwordx4 v[2:3], off
	s_add_i32 m0, s31, 0x1c000
	v_lshl_add_u64 v[2:3], s[12:13], 0, v[132:133]
	global_load_lds_dwordx4 v[2:3], off
	v_lshl_add_u64 v[2:3], s[12:13], 0, v[136:137]
	s_add_i32 m0, s31, 0x1e000
	s_sext_i32_i8 s57, s4
	global_load_lds_dwordx4 v[2:3], off
	s_waitcnt vmcnt(8)
	s_barrier
	v_and_b32_e32 v2, 15, v0
	v_lshlrev_b32_e32 v3, 1, v13
	v_lshlrev_b32_e32 v4, 2, v0
	v_lshlrev_b32_e32 v5, 6, v0
	s_movk_i32 s4, 0x3c0
	v_lshl_or_b32 v154, s5, 6, v2
	v_lshl_or_b32 v2, v2, 6, v3
	v_and_b32_e32 v4, 32, v4
	v_and_or_b32 v3, v5, s4, v3
	v_bitop3_b32 v155, s15, v3, v4 bitop3:0xf6
	v_lshlrev_b32_e32 v3, 9, v0
	v_bitop3_b32 v2, v2, s11, v4 bitop3:0xde
	v_and_b32_e32 v3, 0x30000, v3
	v_lshlrev_b32_e32 v4, 12, v12
	v_or3_b32 v3, v10, v3, v4
	v_add_u32_e32 v138, v3, v11
	v_lshlrev_b32_e32 v3, 5, v14
	s_waitcnt vmcnt(6)
	s_cmpk_lt_u32 s10, 0x100
	v_and_b32_e32 v3, 0x70000, v3
	s_cselect_b64 s[10:11], -1, 0
	v_or3_b32 v3, v10, v3, v4
	s_add_i32 s55, 0, 0x10000
	s_add_i32 s56, 0, 0x14000
	s_ashr_i32 s54, s88, 31
	v_or_b32_e32 v156, s14, v13
	v_mov_b32_e32 v139, v133
	v_add_u32_e32 v140, v3, v11
	v_mov_b32_e32 v141, v133
	v_mov_b64_e32 v[142:143], 0x200
	v_mov_b64_e32 v[144:145], 0x1ff
	v_add_u32_e32 v157, s55, v155
	v_add_u32_e32 v159, s56, v155
	v_add_u32_e32 v160, 0, v2
	s_mov_b64 s[12:13], 0x40000
	s_mov_b64 s[14:15], 0x48000
	s_mov_b64 s[16:17], 0x50000
	s_mov_b64 s[18:19], 0x58000
	s_barrier
	s_branch .LBB0_841

.LBB0_1076:
	s_add_u32 s6, s46, 0x800000
	s_addc_u32 s7, s47, 0
	s_lshl_b32 s8, s8, 5
	s_and_b32 s14, s8, 0x60
	s_mov_b64 s[8:9], 0x80
	s_add_i32 m0, s25, 0x18000
	v_lshl_add_u64 v[8:9], v[8:9], 0, s[8:9]
	s_lshl_b32 s12, s3, 13
	s_lshl_b32 s16, s14, 7
	global_load_lds_dwordx4 v[8:9], off
	v_lshl_add_u64 v[6:7], v[6:7], 0, s[8:9]
	s_add_i32 m0, s25, 0x1a000
	s_add_i32 s50, s25, 0x8000
	s_add_i32 s51, s25, 0xa000
	global_load_lds_dwordx4 v[6:7], off
	v_lshl_add_u64 v[2:3], v[2:3], 0, s[8:9]
	s_mov_b32 m0, s50
	s_add_u32 s10, s30, 0x40080
	global_load_lds_dwordx4 v[2:3], off
	v_lshl_add_u64 v[2:3], v[4:5], 0, s[8:9]
	s_mov_b32 m0, s51
	s_addc_u32 s11, s31, 0
	global_load_lds_dwordx4 v[2:3], off
	s_add_i32 m0, s25, 0x1c000
	v_lshl_add_u64 v[2:3], s[10:11], 0, v[132:133]
	global_load_lds_dwordx4 v[2:3], off
	v_lshl_add_u64 v[2:3], s[10:11], 0, v[140:141]
	s_add_i32 m0, s25, 0x1e000
	v_lshlrev_b32_e32 v4, 2, v0
	global_load_lds_dwordx4 v[2:3], off
	s_waitcnt vmcnt(8)
	s_barrier
	v_and_b32_e32 v2, 15, v0
	v_lshl_or_b32 v1, s3, 6, v2
	v_lshlrev_b32_e32 v3, 1, v14
	v_lshlrev_b32_e32 v5, 6, v0
	s_movk_i32 s3, 0x3c0
	v_lshl_or_b32 v2, v2, 6, v3
	v_and_b32_e32 v4, 32, v4
	v_and_or_b32 v3, v5, s3, v3
	v_bitop3_b32 v135, s16, v3, v4 bitop3:0xf6
	v_lshlrev_b32_e32 v3, 8, v0
	v_bitop3_b32 v2, v2, s12, v4 bitop3:0xde
	v_and_b32_e32 v3, 0x18000, v3
	v_lshlrev_b32_e32 v4, 11, v13
	v_or3_b32 v3, v12, v3, v4
	v_add_u32_e32 v142, v3, v11
	v_lshlrev_b32_e32 v3, 4, v10
	s_waitcnt vmcnt(6)
	s_cmpk_lt_u32 s2, 0x100
	v_and_b32_e32 v3, 0x38000, v3
	s_cselect_b64 s[10:11], -1, 0
	v_or3_b32 v3, v12, v3, v4
	s_add_i32 s53, 0, 0x10000
	s_add_i32 s54, 0, 0x14000
	s_ashr_i32 s52, s88, 31
	v_ashrrev_i32_e32 v131, 31, v130
	v_or_b32_e32 v147, s14, v14
	v_mov_b32_e32 v143, v133
	v_add_u32_e32 v144, v3, v11
	v_mov_b32_e32 v145, v133
	v_add_u32_e32 v152, s53, v135
	v_add_u32_e32 v153, s54, v135
	v_add_u32_e32 v154, 0, v2
	v_mov_b32_e32 v155, 0x7f7f7f7f
	v_mov_b32_e32 v156, 0x78787878
	s_movk_i32 s55, 0x1c00
	s_mov_b32 s12, 0xbfb8aa3b
	s_mov_b32 s14, 0x3e000000
	s_mov_b32 s56, 0xc3e00000
	v_mov_b32_e32 v157, 0x43e00000
	s_barrier
	s_branch .LBB0_1079

.LBB0_1149:
	s_add_u32 s12, s46, 0x33e00000
	s_addc_u32 s13, s47, 0
	s_lshl_b32 s14, s14, 5
	s_and_b32 s18, s14, 0x60
	s_mov_b64 s[14:15], 0x80
	s_add_i32 m0, s51, 0x18000
	v_lshl_add_u64 v[8:9], v[8:9], 0, s[14:15]
	s_lshl_b32 s1, s3, 13
	global_load_lds_dwordx4 v[8:9], off
	v_lshl_add_u64 v[6:7], v[6:7], 0, s[14:15]
	s_add_i32 m0, s51, 0x1a000
	s_add_i32 s56, s51, 0x8000
	s_add_i32 s57, s51, 0xa000
	global_load_lds_dwordx4 v[6:7], off
	v_lshl_add_u64 v[2:3], v[2:3], 0, s[14:15]
	s_mov_b32 m0, s56
	s_add_u32 s16, s38, 0xe0080
	global_load_lds_dwordx4 v[2:3], off
	v_lshl_add_u64 v[2:3], v[4:5], 0, s[14:15]
	s_mov_b32 m0, s57
	s_addc_u32 s17, s39, 0
	global_load_lds_dwordx4 v[2:3], off
	s_add_i32 m0, s51, 0x1c000
	v_lshl_add_u64 v[2:3], s[16:17], 0, v[130:131]
	global_load_lds_dwordx4 v[2:3], off
	v_lshl_add_u64 v[2:3], s[16:17], 0, v[138:139]
	s_add_i32 m0, s51, 0x1e000
	s_cmpk_lt_u32 s2, 0x100
	global_load_lds_dwordx4 v[2:3], off
	s_waitcnt vmcnt(8)
	s_barrier
	v_lshlrev_b32_e32 v3, 2, v150
	v_lshl_or_b32 v2, v150, 6, v154
	v_and_b32_e32 v3, 32, v3
	v_bitop3_b32 v2, v2, s1, v3 bitop3:0xde
	s_waitcnt vmcnt(6)
	v_add_u16_e32 v3, v10, v152
	v_lshl_or_b32 v158, s18, 7, v153
	s_cselect_b64 s[16:17], -1, 0
	v_lshrrev_b16_e32 v3, 1, v3
	s_add_i32 s58, 0, 0x10000
	s_add_i32 s59, 0, 0x14000
	v_lshl_or_b32 v157, s3, 6, v150
	v_or_b32_e32 v159, s18, v151
	v_add_lshl_u32 v140, v11, v3, 1
	v_mov_b32_e32 v141, v131
	v_add_lshl_u32 v142, v12, v3, 1
	v_mov_b32_e32 v143, v131
	v_add_u32_e32 v160, s58, v158
	v_add_u32_e32 v161, s59, v158
	v_add_u32_e32 v162, 0, v2
	v_mov_b32_e32 v164, 0x7c7c7c7c
	v_mov_b32_e32 v165, 0x78787878
	s_mov_b64 s[18:19], 0x80000
	s_mov_b32 s60, 0x80000
	s_mov_b64 s[20:21], 0x90000
	s_mov_b32 s61, 0x90000
	s_mov_b64 s[22:23], 0xa0000
	s_mov_b32 s62, 0xa0000
	s_mov_b64 s[24:25], 0xb0000
	s_mov_b32 s63, 0xb0000
	s_add_i32 s64, s51, 0xc000
	s_add_i32 s65, s51, 0xe000
	s_barrier
	s_branch .LBB0_1152

.LBB0_1169:
	s_mul_i32 s11, s9, s31
	s_sub_i32 s11, 0xe00, s11
	s_add_i32 s12, s9, 1
	s_sub_i32 s13, s11, s31
	s_cmp_ge_u32 s11, s31
	s_cselect_b32 s9, s12, s9
	s_cselect_b32 s11, s13, s11
	s_add_i32 s12, s9, 1
	s_cmp_ge_u32 s11, s31
	s_cselect_b32 s9, s12, s9
	s_xor_b32 s9, s9, s35
	s_sub_i32 s11, s9, s35
	s_add_u32 s50, s46, 0x66600000
	s_addc_u32 s51, s47, 0
	s_lshl_b32 s52, s3, 8
	s_cmp_eq_u32 s30, 7
	s_mov_b32 s3, 0x880000
	s_cselect_b32 s53, s3, 0xf80000
	s_bfe_u32 s3, s11, 0x60019
	s_lshl_b32 s8, s8, 5
	s_add_i32 s3, s11, s3
	s_and_b32 s14, s8, 0x60
	s_mov_b64 s[8:9], 0x80
	s_sext_i32_i16 s3, s3
	s_add_i32 m0, s21, 0x18000
	v_lshl_add_u64 v[6:7], v[6:7], 0, s[8:9]
	s_ashr_i32 s54, s3, 6
	s_lshl_b32 s3, s10, 13
	global_load_lds_dwordx4 v[6:7], off
	v_lshl_add_u64 v[4:5], v[4:5], 0, s[8:9]
	s_add_i32 m0, s21, 0x1a000
	s_add_i32 s55, s21, 0x8000
	s_add_i32 s56, s21, 0xa000
	global_load_lds_dwordx4 v[4:5], off
	v_lshl_add_u64 v[0:1], v[0:1], 0, s[8:9]
	s_mov_b32 m0, s55
	s_add_u32 s12, s24, 0xe0080
	global_load_lds_dwordx4 v[0:1], off
	v_lshl_add_u64 v[0:1], v[2:3], 0, s[8:9]
	s_mov_b32 m0, s56
	s_addc_u32 s13, s25, 0
	global_load_lds_dwordx4 v[0:1], off
	s_add_i32 m0, s21, 0x1c000
	v_lshl_add_u64 v[0:1], s[12:13], 0, v[128:129]
	global_load_lds_dwordx4 v[0:1], off
	v_lshl_add_u64 v[0:1], s[12:13], 0, v[134:135]
	s_add_i32 m0, s21, 0x1e000
	s_cmp_gt_i32 s11, 63
	global_load_lds_dwordx4 v[0:1], off
	s_waitcnt vmcnt(8)
	s_barrier
	v_lshl_or_b32 v147, s10, 6, v150
	s_cselect_b64 s[10:11], -1, 0
	s_add_i32 s58, s54, -2
	s_cmpk_lt_u32 s2, 0x100
	s_cselect_b64 s[12:13], -1, 0
	s_abs_i32 s59, s37
	v_cvt_f32_u32_e32 v1, s59
	v_lshlrev_b32_e32 v2, 2, v150
	v_lshl_or_b32 v0, v150, 6, v154
	v_and_b32_e32 v2, 32, v2
	v_rcp_iflag_f32_e32 v1, v1
	v_bitop3_b32 v0, v0, s3, v2 bitop3:0xde
	s_sub_i32 s2, 0, s59
	s_waitcnt vmcnt(6)
	v_mul_f32_e32 v1, 0x4f7ffffe, v1
	v_cvt_u32_f32_e32 v1, v1
	v_lshl_or_b32 v150, s14, 7, v153
	s_add_i32 s62, 0, 0x10000
	s_add_i32 s63, 0, 0x14000
	v_readfirstlane_b32 s3, v1
	s_mul_i32 s2, s2, s3
	v_add_u16_e32 v1, v8, v152
	s_mul_hi_u32 s2, s3, s2
	v_lshrrev_b16_e32 v1, 1, v1
	s_mov_b32 s57, 0
	v_or_b32_e32 v151, s14, v151
	s_ashr_i32 s60, s37, 31
	s_add_i32 s61, s3, s2
	v_add_lshl_u32 v136, v10, v1, 1
	v_mov_b32_e32 v137, v129
	v_add_lshl_u32 v138, v9, v1, 1
	v_mov_b32_e32 v139, v129
	v_add_u32_e32 v152, s62, v150
	v_add_u32_e32 v153, s63, v150
	v_add_u32_e32 v154, 0, v0
	v_mov_b32_e32 v155, 0x7c7c7c7c
	v_mov_b32_e32 v156, 0x78787878
	s_barrier
	s_branch .LBB0_1172
